# baseline (speedup 1.0000x reference)
.LBB4_5:
	ds_read_b128 v[82:85], v161
	ds_read_b128 v[94:97], v161 offset:2048
	ds_read_b128 v[102:105], v162
	ds_read_b128 v[110:113], v162 offset:2048
	ds_read_b128 v[58:61], v163
	ds_read_b128 v[66:69], v163 offset:2048
	ds_read_b128 v[62:65], v164
	ds_read_b128 v[70:73], v164 offset:2048
	ds_read_b128 v[74:77], v163 offset:4096
	ds_read_b128 v[86:89], v163 offset:6144
	ds_read_b128 v[78:81], v164 offset:4096
	ds_read_b128 v[90:93], v164 offset:6144
	s_waitcnt lgkmcnt(8)
	ds_read_b128 v[142:145], v161 offset:16384
	ds_read_b128 v[166:169], v161 offset:18432
	ds_read_b128 v[170:173], v162 offset:16384
	ds_read_b128 v[174:177], v162 offset:18432
	s_add_i32 s53, s53, 1
	s_mul_i32 s0, s53, s72
	s_mul_hi_u32 s1, s53, s33
	s_add_i32 s1, s1, s0
	s_mul_i32 s0, s53, s33
	s_add_u32 s4, s0, s2
	s_addc_u32 s5, s1, s73
	v_mov_b64_e32 v[156:157], s[20:21]
	v_cmp_ge_i64_e32 vcc, s[4:5], v[156:157]
	s_and_b64 s[0:1], exec, vcc
	s_mov_b64 vcc, s[0:1]
	s_cbranch_vccnz .LBB4_7
	s_and_b32 s13, s4, 7
	s_lshl_b32 s13, s13, s50
	s_ashr_i32 s28, s4, 3
	s_add_i32 s13, s13, s28
	s_ashr_i32 s28, s13, s51
	s_and_b32 s13, s13, s62
	s_lshl_b32 s28, s28, 3
	s_and_b32 s29, s13, 7
	s_or_b32 s74, s28, s29
	s_ashr_i32 s28, s74, s52
	s_lshr_b32 s13, s13, 3
	s_mul_i32 s28, s28, s6
	s_and_b32 s75, s74, s7
	s_add_i32 s28, s28, s13

.Lrs_a_4:
	s_add_u32 s81, s40, s22
	s_addc_u32 s82, s41, s23
	s_add_u32 s29, s40, 0x100
	s_addc_u32 s44, s41, 0
	s_and_b64 s[42:43], s[14:15], exec
	s_cselect_b32 s47, s37, s44
	s_cselect_b32 s46, s36, s29
	s_add_u32 s29, s38, 0x100
	s_addc_u32 s44, s39, 0
	s_and_b64 s[42:43], s[14:15], exec
	s_cselect_b32 s49, s5, s44
	s_cselect_b32 s48, s4, s29
	s_add_u32 s44, s46, 0x80
	s_addc_u32 s45, s47, 0
	s_add_u32 s42, s48, 0x80
	s_addc_u32 s43, s49, 0
	s_add_u32 s78, s81, 0x80
	s_addc_u32 s79, s82, 0
	s_mov_b32 m0, s70
	s_nop 0
	global_load_lds_dwordx4 v146, s[78:79]
	s_mov_b32 m0, s71
	s_nop 0
	global_load_lds_dwordx4 v150, s[78:79]
	s_waitcnt vmcnt(8)
	s_waitcnt lgkmcnt(0)
	s_barrier
	s_waitcnt lgkmcnt(0)
	s_waitcnt vmcnt(16)
	v_mov_b32_e32 v1, v0
	v_pk_mul_f32 v[16:17], v[0:1], v[16:17]
	v_pk_mul_f32 v[14:15], v[154:155], v[14:15]
	v_pk_mul_f32 v[12:13], v[0:1], v[12:13]
	v_pk_mul_f32 v[10:11], v[154:155], v[10:11]
	v_pk_mul_f32 v[8:9], v[0:1], v[8:9]
	v_pk_mul_f32 v[6:7], v[154:155], v[6:7]
	v_pk_mul_f32 v[4:5], v[0:1], v[4:5]
	v_pk_mul_f32 v[2:3], v[154:155], v[2:3]
	s_setprio 1
	s_waitcnt lgkmcnt(7)
	v_mfma_f32_16x16x128_f8f6f4 v[18:21], v[82:85], v[58:61], v[14:17] cbsz:4 blgp:4
	s_waitcnt lgkmcnt(5)
	v_mfma_f32_16x16x128_f8f6f4 v[18:21], v[102:105], v[62:65], v[18:21] cbsz:4 blgp:4
	v_mfma_f32_16x16x128_f8f6f4 v[22:25], v[94:97], v[58:61], v[10:13] cbsz:4 blgp:4
	s_nop 0
	v_mfma_f32_16x16x128_f8f6f4 v[22:25], v[110:113], v[62:65], v[22:25] cbsz:4 blgp:4
	v_mfma_f32_16x16x128_f8f6f4 v[26:29], v[82:85], v[66:69], v[14:17] cbsz:4 blgp:4
	s_waitcnt lgkmcnt(4)
	v_mfma_f32_16x16x128_f8f6f4 v[26:29], v[102:105], v[70:73], v[26:29] cbsz:4 blgp:4
	v_mfma_f32_16x16x128_f8f6f4 v[30:33], v[94:97], v[66:69], v[10:13] cbsz:4 blgp:4
	s_nop 0
	v_mfma_f32_16x16x128_f8f6f4 v[30:33], v[110:113], v[70:73], v[30:33] cbsz:4 blgp:4
	s_waitcnt lgkmcnt(3)
	v_mfma_f32_16x16x128_f8f6f4 v[34:37], v[82:85], v[74:77], v[14:17] cbsz:4 blgp:4
	s_waitcnt lgkmcnt(1)
	v_mfma_f32_16x16x128_f8f6f4 v[34:37], v[102:105], v[78:81], v[34:37] cbsz:4 blgp:4
	v_mfma_f32_16x16x128_f8f6f4 v[38:41], v[94:97], v[74:77], v[10:13] cbsz:4 blgp:4
	s_nop 0
	v_mfma_f32_16x16x128_f8f6f4 v[38:41], v[110:113], v[78:81], v[38:41] cbsz:4 blgp:4
	v_mfma_f32_16x16x128_f8f6f4 v[42:45], v[82:85], v[86:89], v[14:17] cbsz:4 blgp:4
	s_waitcnt lgkmcnt(0)
	v_mfma_f32_16x16x128_f8f6f4 v[42:45], v[102:105], v[90:93], v[42:45] cbsz:4 blgp:4
	v_mfma_f32_16x16x128_f8f6f4 v[46:49], v[94:97], v[86:89], v[10:13] cbsz:4 blgp:4
	s_nop 0
	v_mfma_f32_16x16x128_f8f6f4 v[46:49], v[110:113], v[90:93], v[46:49] cbsz:4 blgp:4
	s_waitcnt lgkmcnt(3)
	v_mfma_f32_16x16x128_f8f6f4 v[50:53], v[142:145], v[58:61], v[6:9] cbsz:4 blgp:4
	s_waitcnt lgkmcnt(1)
	v_mfma_f32_16x16x128_f8f6f4 v[50:53], v[170:173], v[62:65], v[50:53] cbsz:4 blgp:4
	v_mfma_f32_16x16x128_f8f6f4 v[54:57], v[166:169], v[58:61], v[2:5] cbsz:4 blgp:4
	s_waitcnt lgkmcnt(0)
	v_mfma_f32_16x16x128_f8f6f4 v[54:57], v[174:177], v[62:65], v[54:57] cbsz:4 blgp:4
	v_mfma_f32_16x16x128_f8f6f4 v[58:61], v[142:145], v[66:69], v[6:9] cbsz:4 blgp:4
	s_nop 0
	v_mfma_f32_16x16x128_f8f6f4 v[58:61], v[170:173], v[70:73], v[58:61] cbsz:4 blgp:4
	v_mfma_f32_16x16x128_f8f6f4 v[62:65], v[166:169], v[66:69], v[2:5] cbsz:4 blgp:4
	s_nop 0
	v_mfma_f32_16x16x128_f8f6f4 v[62:65], v[174:177], v[70:73], v[62:65] cbsz:4 blgp:4
	v_mfma_f32_16x16x128_f8f6f4 v[66:69], v[142:145], v[74:77], v[6:9] cbsz:4 blgp:4
	s_nop 0
	v_mfma_f32_16x16x128_f8f6f4 v[66:69], v[170:173], v[78:81], v[66:69] cbsz:4 blgp:4
	v_mfma_f32_16x16x128_f8f6f4 v[70:73], v[166:169], v[74:77], v[2:5] cbsz:4 blgp:4
	s_nop 0
	v_mfma_f32_16x16x128_f8f6f4 v[70:73], v[174:177], v[78:81], v[70:73] cbsz:4 blgp:4
	v_mfma_f32_16x16x128_f8f6f4 v[74:77], v[142:145], v[86:89], v[6:9] cbsz:4 blgp:4
	s_nop 0
	v_mfma_f32_16x16x128_f8f6f4 v[74:77], v[170:173], v[90:93], v[74:77] cbsz:4 blgp:4
	v_mfma_f32_16x16x128_f8f6f4 v[78:81], v[166:169], v[86:89], v[2:5] cbsz:4 blgp:4
	s_nop 0
	v_mfma_f32_16x16x128_f8f6f4 v[78:81], v[174:177], v[90:93], v[78:81] cbsz:4 blgp:4
	s_setprio 0
	s_barrier
	s_mov_b32 m0, s55
	s_nop 0
	global_load_lds_dwordx4 v148, s[48:49]
	s_mov_b32 m0, s56
	s_nop 0
	global_load_lds_dwordx4 v152, s[48:49]
	ds_read_b128 v[114:117], v163 offset:16384
	ds_read_b128 v[122:125], v163 offset:18432
	ds_read_b128 v[130:133], v164 offset:16384
	ds_read_b128 v[134:137], v164 offset:18432
	ds_read_b128 v[178:181], v163 offset:20480
	ds_read_b128 v[182:185], v163 offset:22528
	ds_read_b128 v[186:189], v164 offset:20480
	ds_read_b128 v[190:193], v164 offset:22528
	s_mov_b32 m0, s54
	s_nop 0
	global_load_lds_dwordx4 v146, s[46:47]
	s_mov_b32 m0, s57
	s_nop 0
	global_load_lds_dwordx4 v150, s[46:47]
	s_add_u32 s48, s48, s24
	s_addc_u32 s49, s49, s25
	s_mov_b32 m0, s58
	s_nop 0
	global_load_lds_dwordx4 v148, s[48:49]
	s_mov_b32 m0, s59
	s_nop 0
	global_load_lds_dwordx4 v152, s[48:49]
	s_waitcnt vmcnt(8)
	s_waitcnt lgkmcnt(0)
	s_barrier
	s_setprio 1
	s_waitcnt lgkmcnt(7)
	v_mfma_f32_16x16x128_f8f6f4 v[86:89], v[82:85], v[114:117], v[14:17] cbsz:4 blgp:4
	s_waitcnt lgkmcnt(5)
	v_mfma_f32_16x16x128_f8f6f4 v[86:89], v[102:105], v[130:133], v[86:89] cbsz:4 blgp:4
	v_mfma_f32_16x16x128_f8f6f4 v[90:93], v[94:97], v[114:117], v[10:13] cbsz:4 blgp:4
	s_nop 0
	v_mfma_f32_16x16x128_f8f6f4 v[90:93], v[110:113], v[130:133], v[90:93] cbsz:4 blgp:4
	v_mfma_f32_16x16x128_f8f6f4 v[98:101], v[82:85], v[122:125], v[14:17] cbsz:4 blgp:4
	s_waitcnt lgkmcnt(4)
	v_mfma_f32_16x16x128_f8f6f4 v[98:101], v[102:105], v[134:137], v[98:101] cbsz:4 blgp:4
	v_mfma_f32_16x16x128_f8f6f4 v[106:109], v[94:97], v[122:125], v[10:13] cbsz:4 blgp:4
	s_nop 0
	v_mfma_f32_16x16x128_f8f6f4 v[106:109], v[110:113], v[134:137], v[106:109] cbsz:4 blgp:4
	s_waitcnt lgkmcnt(3)
	v_mfma_f32_16x16x128_f8f6f4 v[118:121], v[82:85], v[178:181], v[14:17] cbsz:4 blgp:4
	s_waitcnt lgkmcnt(1)
	v_mfma_f32_16x16x128_f8f6f4 v[118:121], v[102:105], v[186:189], v[118:121] cbsz:4 blgp:4
	v_mfma_f32_16x16x128_f8f6f4 v[126:129], v[94:97], v[178:181], v[10:13] cbsz:4 blgp:4
	s_nop 0
	v_mfma_f32_16x16x128_f8f6f4 v[126:129], v[110:113], v[186:189], v[126:129] cbsz:4 blgp:4
	v_mfma_f32_16x16x128_f8f6f4 v[138:141], v[82:85], v[182:185], v[14:17] cbsz:4 blgp:4
	s_waitcnt lgkmcnt(0)
	v_mfma_f32_16x16x128_f8f6f4 v[138:141], v[102:105], v[190:193], v[138:141] cbsz:4 blgp:4
	v_mfma_f32_16x16x128_f8f6f4 v[82:85], v[94:97], v[182:185], v[10:13] cbsz:4 blgp:4
	s_nop 0
	v_mfma_f32_16x16x128_f8f6f4 v[82:85], v[110:113], v[190:193], v[82:85] cbsz:4 blgp:4
	v_mfma_f32_16x16x128_f8f6f4 v[94:97], v[142:145], v[114:117], v[6:9] cbsz:4 blgp:4
	s_nop 0
	v_mfma_f32_16x16x128_f8f6f4 v[94:97], v[170:173], v[130:133], v[94:97] cbsz:4 blgp:4
	v_mfma_f32_16x16x128_f8f6f4 v[102:105], v[166:169], v[114:117], v[2:5] cbsz:4 blgp:4
	s_nop 0
	v_mfma_f32_16x16x128_f8f6f4 v[102:105], v[174:177], v[130:133], v[102:105] cbsz:4 blgp:4
	v_mfma_f32_16x16x128_f8f6f4 v[110:113], v[142:145], v[122:125], v[6:9] cbsz:4 blgp:4
	s_nop 0
	v_mfma_f32_16x16x128_f8f6f4 v[110:113], v[170:173], v[134:137], v[110:113] cbsz:4 blgp:4
	v_mfma_f32_16x16x128_f8f6f4 v[114:117], v[166:169], v[122:125], v[2:5] cbsz:4 blgp:4
	s_nop 0
	v_mfma_f32_16x16x128_f8f6f4 v[114:117], v[174:177], v[134:137], v[114:117] cbsz:4 blgp:4
	v_mfma_f32_16x16x128_f8f6f4 v[122:125], v[142:145], v[178:181], v[6:9] cbsz:4 blgp:4
	s_nop 0
	v_mfma_f32_16x16x128_f8f6f4 v[122:125], v[170:173], v[186:189], v[122:125] cbsz:4 blgp:4
	v_mfma_f32_16x16x128_f8f6f4 v[130:133], v[166:169], v[178:181], v[2:5] cbsz:4 blgp:4
	s_nop 0
	v_mfma_f32_16x16x128_f8f6f4 v[130:133], v[174:177], v[186:189], v[130:133] cbsz:4 blgp:4
	v_mfma_f32_16x16x128_f8f6f4 v[134:137], v[142:145], v[182:185], v[6:9] cbsz:4 blgp:4
	s_nop 0
	v_mfma_f32_16x16x128_f8f6f4 v[134:137], v[170:173], v[190:193], v[134:137] cbsz:4 blgp:4
	v_mfma_f32_16x16x128_f8f6f4 v[142:145], v[166:169], v[182:185], v[2:5] cbsz:4 blgp:4
	s_nop 0
	v_mfma_f32_16x16x128_f8f6f4 v[142:145], v[174:177], v[190:193], v[142:145] cbsz:4 blgp:4
	s_setprio 0
	s_barrier
	ds_read_b128 v[166:169], v161 offset:32768
	ds_read_b128 v[170:173], v161 offset:34816
	ds_read_b128 v[174:177], v162 offset:32768
	ds_read_b128 v[178:181], v162 offset:34816
	ds_read_b128 v[182:185], v163 offset:32768
	ds_read_b128 v[186:189], v163 offset:34816
	ds_read_b128 v[190:193], v164 offset:32768
	ds_read_b128 v[194:197], v164 offset:34816
	ds_read_b128 v[198:201], v163 offset:36864
	ds_read_b128 v[202:205], v163 offset:38912
	ds_read_b128 v[206:209], v164 offset:36864
	ds_read_b128 v[210:213], v164 offset:38912
	s_add_u32 s46, s46, s22
	s_addc_u32 s47, s47, s23
	s_mov_b32 m0, s60
	s_nop 0
	global_load_lds_dwordx4 v146, s[46:47]
	s_mov_b32 m0, s61
	s_nop 0
	global_load_lds_dwordx4 v150, s[46:47]
	s_waitcnt lgkmcnt(8)
	ds_read_b128 v[214:217], v161 offset:49152
	ds_read_b128 v[218:221], v161 offset:51200
	ds_read_b128 v[222:225], v162 offset:49152
	ds_read_b128 v[226:229], v162 offset:51200
	s_waitcnt vmcnt(8)
	s_waitcnt lgkmcnt(0)
	s_barrier
	s_waitcnt lgkmcnt(0)
	s_setprio 1
	s_waitcnt lgkmcnt(7)
	v_mfma_f32_16x16x128_f8f6f4 v[18:21], v[166:169], v[182:185], v[18:21] cbsz:4 blgp:4
	s_waitcnt lgkmcnt(5)
	v_mfma_f32_16x16x128_f8f6f4 v[18:21], v[174:177], v[190:193], v[18:21] cbsz:4 blgp:4
	v_mfma_f32_16x16x128_f8f6f4 v[22:25], v[170:173], v[182:185], v[22:25] cbsz:4 blgp:4
	s_nop 0
	v_mfma_f32_16x16x128_f8f6f4 v[22:25], v[178:181], v[190:193], v[22:25] cbsz:4 blgp:4
	v_mfma_f32_16x16x128_f8f6f4 v[26:29], v[166:169], v[186:189], v[26:29] cbsz:4 blgp:4
	s_waitcnt lgkmcnt(4)
	v_mfma_f32_16x16x128_f8f6f4 v[26:29], v[174:177], v[194:197], v[26:29] cbsz:4 blgp:4
	v_mfma_f32_16x16x128_f8f6f4 v[30:33], v[170:173], v[186:189], v[30:33] cbsz:4 blgp:4
	s_nop 0
	v_mfma_f32_16x16x128_f8f6f4 v[30:33], v[178:181], v[194:197], v[30:33] cbsz:4 blgp:4
	s_waitcnt lgkmcnt(3)
	v_mfma_f32_16x16x128_f8f6f4 v[34:37], v[166:169], v[198:201], v[34:37] cbsz:4 blgp:4
	s_waitcnt lgkmcnt(1)
	v_mfma_f32_16x16x128_f8f6f4 v[34:37], v[174:177], v[206:209], v[34:37] cbsz:4 blgp:4
	v_mfma_f32_16x16x128_f8f6f4 v[38:41], v[170:173], v[198:201], v[38:41] cbsz:4 blgp:4
	s_nop 0
	v_mfma_f32_16x16x128_f8f6f4 v[38:41], v[178:181], v[206:209], v[38:41] cbsz:4 blgp:4
	v_mfma_f32_16x16x128_f8f6f4 v[42:45], v[166:169], v[202:205], v[42:45] cbsz:4 blgp:4
	s_waitcnt lgkmcnt(0)
	v_mfma_f32_16x16x128_f8f6f4 v[42:45], v[174:177], v[210:213], v[42:45] cbsz:4 blgp:4
	v_mfma_f32_16x16x128_f8f6f4 v[46:49], v[170:173], v[202:205], v[46:49] cbsz:4 blgp:4
	s_nop 0
	v_mfma_f32_16x16x128_f8f6f4 v[46:49], v[178:181], v[210:213], v[46:49] cbsz:4 blgp:4
	s_waitcnt lgkmcnt(3)
	v_mfma_f32_16x16x128_f8f6f4 v[50:53], v[214:217], v[182:185], v[50:53] cbsz:4 blgp:4
	s_waitcnt lgkmcnt(1)
	v_mfma_f32_16x16x128_f8f6f4 v[50:53], v[222:225], v[190:193], v[50:53] cbsz:4 blgp:4
	v_mfma_f32_16x16x128_f8f6f4 v[54:57], v[218:221], v[182:185], v[54:57] cbsz:4 blgp:4
	s_waitcnt lgkmcnt(0)
	v_mfma_f32_16x16x128_f8f6f4 v[54:57], v[226:229], v[190:193], v[54:57] cbsz:4 blgp:4
	v_mfma_f32_16x16x128_f8f6f4 v[58:61], v[214:217], v[186:189], v[58:61] cbsz:4 blgp:4
	s_nop 0
	v_mfma_f32_16x16x128_f8f6f4 v[58:61], v[222:225], v[194:197], v[58:61] cbsz:4 blgp:4
	v_mfma_f32_16x16x128_f8f6f4 v[62:65], v[218:221], v[186:189], v[62:65] cbsz:4 blgp:4
	s_nop 0
	v_mfma_f32_16x16x128_f8f6f4 v[62:65], v[226:229], v[194:197], v[62:65] cbsz:4 blgp:4
	v_mfma_f32_16x16x128_f8f6f4 v[66:69], v[214:217], v[198:201], v[66:69] cbsz:4 blgp:4
	s_nop 0
	v_mfma_f32_16x16x128_f8f6f4 v[66:69], v[222:225], v[206:209], v[66:69] cbsz:4 blgp:4
	v_mfma_f32_16x16x128_f8f6f4 v[70:73], v[218:221], v[198:201], v[70:73] cbsz:4 blgp:4
	s_nop 0
	v_mfma_f32_16x16x128_f8f6f4 v[70:73], v[226:229], v[206:209], v[70:73] cbsz:4 blgp:4
	v_mfma_f32_16x16x128_f8f6f4 v[74:77], v[214:217], v[202:205], v[74:77] cbsz:4 blgp:4
	s_nop 0
	v_mfma_f32_16x16x128_f8f6f4 v[74:77], v[222:225], v[210:213], v[74:77] cbsz:4 blgp:4
	v_mfma_f32_16x16x128_f8f6f4 v[78:81], v[218:221], v[202:205], v[78:81] cbsz:4 blgp:4
	s_nop 0
	v_mfma_f32_16x16x128_f8f6f4 v[78:81], v[226:229], v[210:213], v[78:81] cbsz:4 blgp:4
	s_setprio 0
	s_barrier
	s_mov_b32 m0, s64
	s_nop 0
	global_load_lds_dwordx4 v148, s[42:43]
	s_mov_b32 m0, s65
	s_nop 0
	global_load_lds_dwordx4 v152, s[42:43]
	ds_read_b128 v[182:185], v163 offset:49152
	ds_read_b128 v[186:189], v163 offset:51200
	ds_read_b128 v[190:193], v164 offset:49152
	ds_read_b128 v[194:197], v164 offset:51200
	ds_read_b128 v[198:201], v163 offset:53248
	ds_read_b128 v[202:205], v163 offset:55296
	ds_read_b128 v[206:209], v164 offset:53248
	ds_read_b128 v[210:213], v164 offset:55296
	s_mov_b32 m0, s66
	s_nop 0
	global_load_lds_dwordx4 v146, s[44:45]
	s_mov_b32 m0, s67
	s_nop 0
	global_load_lds_dwordx4 v150, s[44:45]
	s_add_u32 s42, s42, s24
	s_addc_u32 s43, s43, s25
	s_mov_b32 m0, s68
	s_nop 0
	global_load_lds_dwordx4 v148, s[42:43]
	s_mov_b32 m0, s69
	s_nop 0
	global_load_lds_dwordx4 v152, s[42:43]
	s_waitcnt vmcnt(8)
	s_waitcnt lgkmcnt(0)
	s_barrier
	s_setprio 1
	s_waitcnt lgkmcnt(7)
	v_mfma_f32_16x16x128_f8f6f4 v[86:89], v[166:169], v[182:185], v[86:89] cbsz:4 blgp:4
	s_waitcnt lgkmcnt(5)
	v_mfma_f32_16x16x128_f8f6f4 v[86:89], v[174:177], v[190:193], v[86:89] cbsz:4 blgp:4
	v_mfma_f32_16x16x128_f8f6f4 v[90:93], v[170:173], v[182:185], v[90:93] cbsz:4 blgp:4
	s_nop 0
	v_mfma_f32_16x16x128_f8f6f4 v[90:93], v[178:181], v[190:193], v[90:93] cbsz:4 blgp:4
	v_mfma_f32_16x16x128_f8f6f4 v[98:101], v[166:169], v[186:189], v[98:101] cbsz:4 blgp:4
	s_waitcnt lgkmcnt(4)
	v_mfma_f32_16x16x128_f8f6f4 v[98:101], v[174:177], v[194:197], v[98:101] cbsz:4 blgp:4
	v_mfma_f32_16x16x128_f8f6f4 v[106:109], v[170:173], v[186:189], v[106:109] cbsz:4 blgp:4
	s_nop 0
	v_mfma_f32_16x16x128_f8f6f4 v[106:109], v[178:181], v[194:197], v[106:109] cbsz:4 blgp:4
	s_waitcnt lgkmcnt(3)
	v_mfma_f32_16x16x128_f8f6f4 v[118:121], v[166:169], v[198:201], v[118:121] cbsz:4 blgp:4
	s_waitcnt lgkmcnt(1)
	v_mfma_f32_16x16x128_f8f6f4 v[118:121], v[174:177], v[206:209], v[118:121] cbsz:4 blgp:4
	v_mfma_f32_16x16x128_f8f6f4 v[126:129], v[170:173], v[198:201], v[126:129] cbsz:4 blgp:4
	s_nop 0
	v_mfma_f32_16x16x128_f8f6f4 v[126:129], v[178:181], v[206:209], v[126:129] cbsz:4 blgp:4
	v_mfma_f32_16x16x128_f8f6f4 v[138:141], v[166:169], v[202:205], v[138:141] cbsz:4 blgp:4
	s_waitcnt lgkmcnt(0)
	v_mfma_f32_16x16x128_f8f6f4 v[138:141], v[174:177], v[210:213], v[138:141] cbsz:4 blgp:4
	v_mfma_f32_16x16x128_f8f6f4 v[82:85], v[170:173], v[202:205], v[82:85] cbsz:4 blgp:4
	s_nop 0
	v_mfma_f32_16x16x128_f8f6f4 v[82:85], v[178:181], v[210:213], v[82:85] cbsz:4 blgp:4
	v_mfma_f32_16x16x128_f8f6f4 v[94:97], v[214:217], v[182:185], v[94:97] cbsz:4 blgp:4
	s_nop 0
	v_mfma_f32_16x16x128_f8f6f4 v[94:97], v[222:225], v[190:193], v[94:97] cbsz:4 blgp:4
	v_mfma_f32_16x16x128_f8f6f4 v[102:105], v[218:221], v[182:185], v[102:105] cbsz:4 blgp:4
	s_nop 0
	v_mfma_f32_16x16x128_f8f6f4 v[102:105], v[226:229], v[190:193], v[102:105] cbsz:4 blgp:4
	v_mfma_f32_16x16x128_f8f6f4 v[110:113], v[214:217], v[186:189], v[110:113] cbsz:4 blgp:4
	s_nop 0
	v_mfma_f32_16x16x128_f8f6f4 v[110:113], v[222:225], v[194:197], v[110:113] cbsz:4 blgp:4
	v_mfma_f32_16x16x128_f8f6f4 v[114:117], v[218:221], v[186:189], v[114:117] cbsz:4 blgp:4
	s_nop 0
	v_mfma_f32_16x16x128_f8f6f4 v[114:117], v[226:229], v[194:197], v[114:117] cbsz:4 blgp:4
	v_mfma_f32_16x16x128_f8f6f4 v[122:125], v[214:217], v[198:201], v[122:125] cbsz:4 blgp:4
	s_nop 0
	v_mfma_f32_16x16x128_f8f6f4 v[122:125], v[222:225], v[206:209], v[122:125] cbsz:4 blgp:4
	v_mfma_f32_16x16x128_f8f6f4 v[130:133], v[218:221], v[198:201], v[130:133] cbsz:4 blgp:4
	s_nop 0
	v_mfma_f32_16x16x128_f8f6f4 v[130:133], v[226:229], v[206:209], v[130:133] cbsz:4 blgp:4
	v_mfma_f32_16x16x128_f8f6f4 v[134:137], v[214:217], v[202:205], v[134:137] cbsz:4 blgp:4
	s_nop 0
	v_mfma_f32_16x16x128_f8f6f4 v[134:137], v[222:225], v[210:213], v[134:137] cbsz:4 blgp:4
	v_mfma_f32_16x16x128_f8f6f4 v[142:145], v[218:221], v[202:205], v[142:145] cbsz:4 blgp:4
	s_nop 0
	v_mfma_f32_16x16x128_f8f6f4 v[142:145], v[226:229], v[210:213], v[142:145] cbsz:4 blgp:4
	s_setprio 0
	s_andn2_b64 vcc, exec, s[34:35]
	s_barrier
	s_cbranch_vccnz .LBB4_4
	s_ashr_i32 s29, s28, 31
	s_lshl_b64 s[42:43], s[28:29], 10
	s_add_u32 s42, s10, s42
	s_addc_u32 s43, s11, s43
	s_add_u32 s29, s40, 0x200
	s_addc_u32 s78, s41, 0
	s_add_u32 s79, s38, 0x200
	s_addc_u32 s80, s39, 0
	s_add_u32 s38, s81, 0x180
	s_addc_u32 s39, s82, 0
	s_mov_b32 s81, 4
	s_cmp_eq_u32 s63, s81
	s_cselect_b64 s[40:41], -1, 0
	s_cmp_lg_u32 s63, s81
	s_cbranch_scc1 .LBB4_15

.LBB5_5:
	ds_read_b128 v[82:85], v163
	ds_read_b128 v[94:97], v163 offset:2048
	ds_read_b128 v[102:105], v164
	ds_read_b128 v[110:113], v164 offset:2048
	ds_read_b128 v[58:61], v165
	ds_read_b128 v[66:69], v165 offset:2048
	ds_read_b128 v[62:65], v166
	ds_read_b128 v[70:73], v166 offset:2048
	ds_read_b128 v[74:77], v165 offset:4096
	ds_read_b128 v[86:89], v165 offset:6144
	ds_read_b128 v[78:81], v166 offset:4096
	ds_read_b128 v[90:93], v166 offset:6144
	s_waitcnt lgkmcnt(8)
	ds_read_b128 v[142:145], v163 offset:16384
	ds_read_b128 v[156:159], v163 offset:18432
	ds_read_b128 v[168:171], v164 offset:16384
	ds_read_b128 v[172:175], v164 offset:18432
	s_add_i32 s54, s54, 1
	s_mul_i32 s0, s54, s73
	s_mul_hi_u32 s1, s54, s33
	s_add_i32 s1, s1, s0
	s_mul_i32 s0, s54, s33
	s_add_u32 s4, s0, s2
	s_addc_u32 s5, s1, s74
	v_mov_b64_e32 v[230:231], s[20:21]
	v_cmp_ge_i64_e32 vcc, s[4:5], v[230:231]
	s_and_b64 s[0:1], exec, vcc
	s_mov_b64 vcc, s[0:1]
	s_cbranch_vccnz .LBB5_7
	s_and_b32 s13, s4, 7
	s_lshl_b32 s13, s13, s37
	s_ashr_i32 s28, s4, 3
	s_add_i32 s13, s13, s28
	s_ashr_i32 s28, s13, s52
	s_and_b32 s13, s13, s63
	s_lshl_b32 s28, s28, 3
	s_and_b32 s29, s13, 7
	s_or_b32 s75, s28, s29
	s_ashr_i32 s28, s75, s53
	s_lshr_b32 s13, s13, 3
	s_mul_i32 s28, s28, s6
	s_and_b32 s76, s75, s7
	s_add_i32 s28, s28, s13
.LBB5_7:
	v_mov_b64_e32 v[230:231], s[20:21]
	v_cmp_lt_i64_e32 vcc, s[4:5], v[230:231]
	s_mov_b64 s[38:39], s[42:43]
	s_nop 0
	v_cndmask_b32_e64 v1, 0, 1, vcc
	v_cmp_ne_u32_e64 s[4:5], 1, v1
	s_andn2_b64 vcc, exec, vcc
	s_cbranch_vccz .LBB5_10
	s_and_b64 vcc, exec, s[4:5]
	s_mov_b64 s[4:5], s[40:41]
	s_cbranch_vccz .LBB5_11

.Lrs_a_5:
	s_add_u32 s82, s42, s22
	s_addc_u32 s83, s43, s23
	s_add_u32 s29, s42, 0x100
	s_addc_u32 s46, s43, 0
	s_and_b64 s[44:45], s[14:15], exec
	s_cselect_b32 s49, s39, s46
	s_cselect_b32 s48, s38, s29
	s_add_u32 s29, s40, 0x100
	s_addc_u32 s46, s41, 0
	s_and_b64 s[44:45], s[14:15], exec
	s_cselect_b32 s51, s5, s46
	s_cselect_b32 s50, s4, s29
	s_add_u32 s46, s48, 0x80
	s_addc_u32 s47, s49, 0
	s_add_u32 s44, s50, 0x80
	s_addc_u32 s45, s51, 0
	s_add_u32 s80, s82, 0x80
	s_addc_u32 s81, s83, 0
	s_mov_b32 m0, s71
	s_nop 0
	global_load_lds_dwordx4 v146, s[80:81]
	s_mov_b32 m0, s72
	s_nop 0
	global_load_lds_dwordx4 v150, s[80:81]
	s_waitcnt vmcnt(8)
	s_waitcnt lgkmcnt(0)
	s_barrier
	s_waitcnt lgkmcnt(0)
	s_waitcnt vmcnt(16)
	v_mov_b32_e32 v1, v0
	v_pk_mul_f32 v[16:17], v[0:1], v[16:17]
	v_pk_mul_f32 v[14:15], v[154:155], v[14:15]
	v_pk_mul_f32 v[12:13], v[0:1], v[12:13]
	v_pk_mul_f32 v[10:11], v[154:155], v[10:11]
	v_pk_mul_f32 v[8:9], v[0:1], v[8:9]
	v_pk_mul_f32 v[6:7], v[154:155], v[6:7]
	v_pk_mul_f32 v[4:5], v[0:1], v[4:5]
	v_pk_mul_f32 v[2:3], v[154:155], v[2:3]
	s_setprio 1
	s_waitcnt lgkmcnt(7)
	v_mfma_f32_16x16x128_f8f6f4 v[18:21], v[82:85], v[58:61], v[14:17] cbsz:4 blgp:4
	s_waitcnt lgkmcnt(5)
	v_mfma_f32_16x16x128_f8f6f4 v[18:21], v[102:105], v[62:65], v[18:21] cbsz:4 blgp:4
	v_mfma_f32_16x16x128_f8f6f4 v[22:25], v[94:97], v[58:61], v[10:13] cbsz:4 blgp:4
	s_nop 0
	v_mfma_f32_16x16x128_f8f6f4 v[22:25], v[110:113], v[62:65], v[22:25] cbsz:4 blgp:4
	v_mfma_f32_16x16x128_f8f6f4 v[26:29], v[82:85], v[66:69], v[14:17] cbsz:4 blgp:4
	s_waitcnt lgkmcnt(4)
	v_mfma_f32_16x16x128_f8f6f4 v[26:29], v[102:105], v[70:73], v[26:29] cbsz:4 blgp:4
	v_mfma_f32_16x16x128_f8f6f4 v[30:33], v[94:97], v[66:69], v[10:13] cbsz:4 blgp:4
	s_nop 0
	v_mfma_f32_16x16x128_f8f6f4 v[30:33], v[110:113], v[70:73], v[30:33] cbsz:4 blgp:4
	s_waitcnt lgkmcnt(3)
	v_mfma_f32_16x16x128_f8f6f4 v[34:37], v[82:85], v[74:77], v[14:17] cbsz:4 blgp:4
	s_waitcnt lgkmcnt(1)
	v_mfma_f32_16x16x128_f8f6f4 v[34:37], v[102:105], v[78:81], v[34:37] cbsz:4 blgp:4
	v_mfma_f32_16x16x128_f8f6f4 v[38:41], v[94:97], v[74:77], v[10:13] cbsz:4 blgp:4
	s_nop 0
	v_mfma_f32_16x16x128_f8f6f4 v[38:41], v[110:113], v[78:81], v[38:41] cbsz:4 blgp:4
	v_mfma_f32_16x16x128_f8f6f4 v[42:45], v[82:85], v[86:89], v[14:17] cbsz:4 blgp:4
	s_waitcnt lgkmcnt(0)
	v_mfma_f32_16x16x128_f8f6f4 v[42:45], v[102:105], v[90:93], v[42:45] cbsz:4 blgp:4
	v_mfma_f32_16x16x128_f8f6f4 v[46:49], v[94:97], v[86:89], v[10:13] cbsz:4 blgp:4
	s_nop 0
	v_mfma_f32_16x16x128_f8f6f4 v[46:49], v[110:113], v[90:93], v[46:49] cbsz:4 blgp:4
	s_waitcnt lgkmcnt(3)
	v_mfma_f32_16x16x128_f8f6f4 v[50:53], v[142:145], v[58:61], v[6:9] cbsz:4 blgp:4
	s_waitcnt lgkmcnt(1)
	v_mfma_f32_16x16x128_f8f6f4 v[50:53], v[168:171], v[62:65], v[50:53] cbsz:4 blgp:4
	v_mfma_f32_16x16x128_f8f6f4 v[54:57], v[156:159], v[58:61], v[2:5] cbsz:4 blgp:4
	s_waitcnt lgkmcnt(0)
	v_mfma_f32_16x16x128_f8f6f4 v[54:57], v[172:175], v[62:65], v[54:57] cbsz:4 blgp:4
	v_mfma_f32_16x16x128_f8f6f4 v[58:61], v[142:145], v[66:69], v[6:9] cbsz:4 blgp:4
	s_nop 0
	v_mfma_f32_16x16x128_f8f6f4 v[58:61], v[168:171], v[70:73], v[58:61] cbsz:4 blgp:4
	v_mfma_f32_16x16x128_f8f6f4 v[62:65], v[156:159], v[66:69], v[2:5] cbsz:4 blgp:4
	s_nop 0
	v_mfma_f32_16x16x128_f8f6f4 v[62:65], v[172:175], v[70:73], v[62:65] cbsz:4 blgp:4
	v_mfma_f32_16x16x128_f8f6f4 v[66:69], v[142:145], v[74:77], v[6:9] cbsz:4 blgp:4
	s_nop 0
	v_mfma_f32_16x16x128_f8f6f4 v[66:69], v[168:171], v[78:81], v[66:69] cbsz:4 blgp:4
	v_mfma_f32_16x16x128_f8f6f4 v[70:73], v[156:159], v[74:77], v[2:5] cbsz:4 blgp:4
	s_nop 0
	v_mfma_f32_16x16x128_f8f6f4 v[70:73], v[172:175], v[78:81], v[70:73] cbsz:4 blgp:4
	v_mfma_f32_16x16x128_f8f6f4 v[74:77], v[142:145], v[86:89], v[6:9] cbsz:4 blgp:4
	s_nop 0
	v_mfma_f32_16x16x128_f8f6f4 v[74:77], v[168:171], v[90:93], v[74:77] cbsz:4 blgp:4
	v_mfma_f32_16x16x128_f8f6f4 v[78:81], v[156:159], v[86:89], v[2:5] cbsz:4 blgp:4
	s_nop 0
	v_mfma_f32_16x16x128_f8f6f4 v[78:81], v[172:175], v[90:93], v[78:81] cbsz:4 blgp:4
	s_setprio 0
	s_barrier
	s_mov_b32 m0, s56
	s_nop 0
	global_load_lds_dwordx4 v148, s[50:51]
	s_mov_b32 m0, s57
	s_nop 0
	global_load_lds_dwordx4 v152, s[50:51]
	ds_read_b128 v[114:117], v165 offset:16384
	ds_read_b128 v[122:125], v165 offset:18432
	ds_read_b128 v[130:133], v166 offset:16384
	ds_read_b128 v[134:137], v166 offset:18432
	ds_read_b128 v[176:179], v165 offset:20480
	ds_read_b128 v[180:183], v165 offset:22528
	ds_read_b128 v[184:187], v166 offset:20480
	ds_read_b128 v[188:191], v166 offset:22528
	s_mov_b32 m0, s55
	s_nop 0
	global_load_lds_dwordx4 v146, s[48:49]
	s_mov_b32 m0, s58
	s_nop 0
	global_load_lds_dwordx4 v150, s[48:49]
	s_add_u32 s50, s50, s24
	s_addc_u32 s51, s51, s25
	s_mov_b32 m0, s59
	s_nop 0
	global_load_lds_dwordx4 v148, s[50:51]
	s_mov_b32 m0, s60
	s_nop 0
	global_load_lds_dwordx4 v152, s[50:51]
	s_waitcnt vmcnt(8)
	s_waitcnt lgkmcnt(0)
	s_barrier
	s_setprio 1
	s_waitcnt lgkmcnt(7)
	v_mfma_f32_16x16x128_f8f6f4 v[86:89], v[82:85], v[114:117], v[14:17] cbsz:4 blgp:4
	s_waitcnt lgkmcnt(5)
	v_mfma_f32_16x16x128_f8f6f4 v[86:89], v[102:105], v[130:133], v[86:89] cbsz:4 blgp:4
	v_mfma_f32_16x16x128_f8f6f4 v[90:93], v[94:97], v[114:117], v[10:13] cbsz:4 blgp:4
	s_nop 0
	v_mfma_f32_16x16x128_f8f6f4 v[90:93], v[110:113], v[130:133], v[90:93] cbsz:4 blgp:4
	v_mfma_f32_16x16x128_f8f6f4 v[98:101], v[82:85], v[122:125], v[14:17] cbsz:4 blgp:4
	s_waitcnt lgkmcnt(4)
	v_mfma_f32_16x16x128_f8f6f4 v[98:101], v[102:105], v[134:137], v[98:101] cbsz:4 blgp:4
	v_mfma_f32_16x16x128_f8f6f4 v[106:109], v[94:97], v[122:125], v[10:13] cbsz:4 blgp:4
	s_nop 0
	v_mfma_f32_16x16x128_f8f6f4 v[106:109], v[110:113], v[134:137], v[106:109] cbsz:4 blgp:4
	s_waitcnt lgkmcnt(3)
	v_mfma_f32_16x16x128_f8f6f4 v[118:121], v[82:85], v[176:179], v[14:17] cbsz:4 blgp:4
	s_waitcnt lgkmcnt(1)
	v_mfma_f32_16x16x128_f8f6f4 v[118:121], v[102:105], v[184:187], v[118:121] cbsz:4 blgp:4
	v_mfma_f32_16x16x128_f8f6f4 v[126:129], v[94:97], v[176:179], v[10:13] cbsz:4 blgp:4
	s_nop 0
	v_mfma_f32_16x16x128_f8f6f4 v[126:129], v[110:113], v[184:187], v[126:129] cbsz:4 blgp:4
	v_mfma_f32_16x16x128_f8f6f4 v[138:141], v[82:85], v[180:183], v[14:17] cbsz:4 blgp:4
	s_waitcnt lgkmcnt(0)
	v_mfma_f32_16x16x128_f8f6f4 v[138:141], v[102:105], v[188:191], v[138:141] cbsz:4 blgp:4
	v_mfma_f32_16x16x128_f8f6f4 v[82:85], v[94:97], v[180:183], v[10:13] cbsz:4 blgp:4
	s_nop 0
	v_mfma_f32_16x16x128_f8f6f4 v[82:85], v[110:113], v[188:191], v[82:85] cbsz:4 blgp:4
	v_mfma_f32_16x16x128_f8f6f4 v[94:97], v[142:145], v[114:117], v[6:9] cbsz:4 blgp:4
	s_nop 0
	v_mfma_f32_16x16x128_f8f6f4 v[94:97], v[168:171], v[130:133], v[94:97] cbsz:4 blgp:4
	v_mfma_f32_16x16x128_f8f6f4 v[102:105], v[156:159], v[114:117], v[2:5] cbsz:4 blgp:4
	s_nop 0
	v_mfma_f32_16x16x128_f8f6f4 v[102:105], v[172:175], v[130:133], v[102:105] cbsz:4 blgp:4
	v_mfma_f32_16x16x128_f8f6f4 v[110:113], v[142:145], v[122:125], v[6:9] cbsz:4 blgp:4
	s_nop 0
	v_mfma_f32_16x16x128_f8f6f4 v[110:113], v[168:171], v[134:137], v[110:113] cbsz:4 blgp:4
	v_mfma_f32_16x16x128_f8f6f4 v[114:117], v[156:159], v[122:125], v[2:5] cbsz:4 blgp:4
	s_nop 0
	v_mfma_f32_16x16x128_f8f6f4 v[114:117], v[172:175], v[134:137], v[114:117] cbsz:4 blgp:4
	v_mfma_f32_16x16x128_f8f6f4 v[122:125], v[142:145], v[176:179], v[6:9] cbsz:4 blgp:4
	s_nop 0
	v_mfma_f32_16x16x128_f8f6f4 v[122:125], v[168:171], v[184:187], v[122:125] cbsz:4 blgp:4
	v_mfma_f32_16x16x128_f8f6f4 v[130:133], v[156:159], v[176:179], v[2:5] cbsz:4 blgp:4
	s_nop 0
	v_mfma_f32_16x16x128_f8f6f4 v[130:133], v[172:175], v[184:187], v[130:133] cbsz:4 blgp:4
	v_mfma_f32_16x16x128_f8f6f4 v[134:137], v[142:145], v[180:183], v[6:9] cbsz:4 blgp:4
	s_nop 0
	v_mfma_f32_16x16x128_f8f6f4 v[134:137], v[168:171], v[188:191], v[134:137] cbsz:4 blgp:4
	v_mfma_f32_16x16x128_f8f6f4 v[142:145], v[156:159], v[180:183], v[2:5] cbsz:4 blgp:4
	s_nop 0
	v_mfma_f32_16x16x128_f8f6f4 v[142:145], v[172:175], v[188:191], v[142:145] cbsz:4 blgp:4
	s_setprio 0
	s_barrier
	ds_read_b128 v[156:159], v163 offset:32768
	ds_read_b128 v[168:171], v163 offset:34816
	ds_read_b128 v[172:175], v164 offset:32768
	ds_read_b128 v[176:179], v164 offset:34816
	ds_read_b128 v[180:183], v165 offset:32768
	ds_read_b128 v[184:187], v165 offset:34816
	ds_read_b128 v[188:191], v166 offset:32768
	ds_read_b128 v[192:195], v166 offset:34816
	ds_read_b128 v[196:199], v165 offset:36864
	ds_read_b128 v[200:203], v165 offset:38912
	ds_read_b128 v[204:207], v166 offset:36864
	ds_read_b128 v[208:211], v166 offset:38912
	s_add_u32 s48, s48, s22
	s_addc_u32 s49, s49, s23
	s_mov_b32 m0, s61
	s_nop 0
	global_load_lds_dwordx4 v146, s[48:49]
	s_mov_b32 m0, s62
	s_nop 0
	global_load_lds_dwordx4 v150, s[48:49]
	s_waitcnt lgkmcnt(8)
	ds_read_b128 v[212:215], v163 offset:49152
	ds_read_b128 v[216:219], v163 offset:51200
	ds_read_b128 v[220:223], v164 offset:49152
	ds_read_b128 v[224:227], v164 offset:51200
	s_waitcnt vmcnt(8)
	s_waitcnt lgkmcnt(0)
	s_barrier
	s_waitcnt lgkmcnt(0)
	s_setprio 1
	s_waitcnt lgkmcnt(7)
	v_mfma_f32_16x16x128_f8f6f4 v[18:21], v[156:159], v[180:183], v[18:21] cbsz:4 blgp:4
	s_waitcnt lgkmcnt(5)
	v_mfma_f32_16x16x128_f8f6f4 v[18:21], v[172:175], v[188:191], v[18:21] cbsz:4 blgp:4
	v_mfma_f32_16x16x128_f8f6f4 v[22:25], v[168:171], v[180:183], v[22:25] cbsz:4 blgp:4
	s_nop 0
	v_mfma_f32_16x16x128_f8f6f4 v[22:25], v[176:179], v[188:191], v[22:25] cbsz:4 blgp:4
	v_mfma_f32_16x16x128_f8f6f4 v[26:29], v[156:159], v[184:187], v[26:29] cbsz:4 blgp:4
	s_waitcnt lgkmcnt(4)
	v_mfma_f32_16x16x128_f8f6f4 v[26:29], v[172:175], v[192:195], v[26:29] cbsz:4 blgp:4
	v_mfma_f32_16x16x128_f8f6f4 v[30:33], v[168:171], v[184:187], v[30:33] cbsz:4 blgp:4
	s_nop 0
	v_mfma_f32_16x16x128_f8f6f4 v[30:33], v[176:179], v[192:195], v[30:33] cbsz:4 blgp:4
	s_waitcnt lgkmcnt(3)
	v_mfma_f32_16x16x128_f8f6f4 v[34:37], v[156:159], v[196:199], v[34:37] cbsz:4 blgp:4
	s_waitcnt lgkmcnt(1)
	v_mfma_f32_16x16x128_f8f6f4 v[34:37], v[172:175], v[204:207], v[34:37] cbsz:4 blgp:4
	v_mfma_f32_16x16x128_f8f6f4 v[38:41], v[168:171], v[196:199], v[38:41] cbsz:4 blgp:4
	s_nop 0
	v_mfma_f32_16x16x128_f8f6f4 v[38:41], v[176:179], v[204:207], v[38:41] cbsz:4 blgp:4
	v_mfma_f32_16x16x128_f8f6f4 v[42:45], v[156:159], v[200:203], v[42:45] cbsz:4 blgp:4
	s_waitcnt lgkmcnt(0)
	v_mfma_f32_16x16x128_f8f6f4 v[42:45], v[172:175], v[208:211], v[42:45] cbsz:4 blgp:4
	v_mfma_f32_16x16x128_f8f6f4 v[46:49], v[168:171], v[200:203], v[46:49] cbsz:4 blgp:4
	s_nop 0
	v_mfma_f32_16x16x128_f8f6f4 v[46:49], v[176:179], v[208:211], v[46:49] cbsz:4 blgp:4
	s_waitcnt lgkmcnt(3)
	v_mfma_f32_16x16x128_f8f6f4 v[50:53], v[212:215], v[180:183], v[50:53] cbsz:4 blgp:4
	s_waitcnt lgkmcnt(1)
	v_mfma_f32_16x16x128_f8f6f4 v[50:53], v[220:223], v[188:191], v[50:53] cbsz:4 blgp:4
	v_mfma_f32_16x16x128_f8f6f4 v[54:57], v[216:219], v[180:183], v[54:57] cbsz:4 blgp:4
	s_waitcnt lgkmcnt(0)
	v_mfma_f32_16x16x128_f8f6f4 v[54:57], v[224:227], v[188:191], v[54:57] cbsz:4 blgp:4
	v_mfma_f32_16x16x128_f8f6f4 v[58:61], v[212:215], v[184:187], v[58:61] cbsz:4 blgp:4
	s_nop 0
	v_mfma_f32_16x16x128_f8f6f4 v[58:61], v[220:223], v[192:195], v[58:61] cbsz:4 blgp:4
	v_mfma_f32_16x16x128_f8f6f4 v[62:65], v[216:219], v[184:187], v[62:65] cbsz:4 blgp:4
	s_nop 0
	v_mfma_f32_16x16x128_f8f6f4 v[62:65], v[224:227], v[192:195], v[62:65] cbsz:4 blgp:4
	v_mfma_f32_16x16x128_f8f6f4 v[66:69], v[212:215], v[196:199], v[66:69] cbsz:4 blgp:4
	s_nop 0
	v_mfma_f32_16x16x128_f8f6f4 v[66:69], v[220:223], v[204:207], v[66:69] cbsz:4 blgp:4
	v_mfma_f32_16x16x128_f8f6f4 v[70:73], v[216:219], v[196:199], v[70:73] cbsz:4 blgp:4
	s_nop 0
	v_mfma_f32_16x16x128_f8f6f4 v[70:73], v[224:227], v[204:207], v[70:73] cbsz:4 blgp:4
	v_mfma_f32_16x16x128_f8f6f4 v[74:77], v[212:215], v[200:203], v[74:77] cbsz:4 blgp:4
	s_nop 0
	v_mfma_f32_16x16x128_f8f6f4 v[74:77], v[220:223], v[208:211], v[74:77] cbsz:4 blgp:4
	v_mfma_f32_16x16x128_f8f6f4 v[78:81], v[216:219], v[200:203], v[78:81] cbsz:4 blgp:4
	s_nop 0
	v_mfma_f32_16x16x128_f8f6f4 v[78:81], v[224:227], v[208:211], v[78:81] cbsz:4 blgp:4
	s_setprio 0
	s_barrier
	s_mov_b32 m0, s65
	s_nop 0
	global_load_lds_dwordx4 v148, s[44:45]
	s_mov_b32 m0, s66
	s_nop 0
	global_load_lds_dwordx4 v152, s[44:45]
	ds_read_b128 v[180:183], v165 offset:49152
	ds_read_b128 v[184:187], v165 offset:51200
	ds_read_b128 v[188:191], v166 offset:49152
	ds_read_b128 v[192:195], v166 offset:51200
	ds_read_b128 v[196:199], v165 offset:53248
	ds_read_b128 v[200:203], v165 offset:55296
	ds_read_b128 v[204:207], v166 offset:53248
	ds_read_b128 v[208:211], v166 offset:55296
	s_mov_b32 m0, s67
	s_nop 0
	global_load_lds_dwordx4 v146, s[46:47]
	s_mov_b32 m0, s68
	s_nop 0
	global_load_lds_dwordx4 v150, s[46:47]
	s_add_u32 s44, s44, s24
	s_addc_u32 s45, s45, s25
	s_mov_b32 m0, s69
	s_nop 0
	global_load_lds_dwordx4 v148, s[44:45]
	s_mov_b32 m0, s70
	s_nop 0
	global_load_lds_dwordx4 v152, s[44:45]
	s_waitcnt vmcnt(8)
	s_waitcnt lgkmcnt(0)
	s_barrier
	s_setprio 1
	s_waitcnt lgkmcnt(7)
	v_mfma_f32_16x16x128_f8f6f4 v[86:89], v[156:159], v[180:183], v[86:89] cbsz:4 blgp:4
	s_waitcnt lgkmcnt(5)
	v_mfma_f32_16x16x128_f8f6f4 v[86:89], v[172:175], v[188:191], v[86:89] cbsz:4 blgp:4
	v_mfma_f32_16x16x128_f8f6f4 v[90:93], v[168:171], v[180:183], v[90:93] cbsz:4 blgp:4
	s_nop 0
	v_mfma_f32_16x16x128_f8f6f4 v[90:93], v[176:179], v[188:191], v[90:93] cbsz:4 blgp:4
	v_mfma_f32_16x16x128_f8f6f4 v[98:101], v[156:159], v[184:187], v[98:101] cbsz:4 blgp:4
	s_waitcnt lgkmcnt(4)
	v_mfma_f32_16x16x128_f8f6f4 v[98:101], v[172:175], v[192:195], v[98:101] cbsz:4 blgp:4
	v_mfma_f32_16x16x128_f8f6f4 v[106:109], v[168:171], v[184:187], v[106:109] cbsz:4 blgp:4
	s_nop 0
	v_mfma_f32_16x16x128_f8f6f4 v[106:109], v[176:179], v[192:195], v[106:109] cbsz:4 blgp:4
	s_waitcnt lgkmcnt(3)
	v_mfma_f32_16x16x128_f8f6f4 v[118:121], v[156:159], v[196:199], v[118:121] cbsz:4 blgp:4
	s_waitcnt lgkmcnt(1)
	v_mfma_f32_16x16x128_f8f6f4 v[118:121], v[172:175], v[204:207], v[118:121] cbsz:4 blgp:4
	v_mfma_f32_16x16x128_f8f6f4 v[126:129], v[168:171], v[196:199], v[126:129] cbsz:4 blgp:4
	s_nop 0
	v_mfma_f32_16x16x128_f8f6f4 v[126:129], v[176:179], v[204:207], v[126:129] cbsz:4 blgp:4
	v_mfma_f32_16x16x128_f8f6f4 v[138:141], v[156:159], v[200:203], v[138:141] cbsz:4 blgp:4
	s_waitcnt lgkmcnt(0)
	v_mfma_f32_16x16x128_f8f6f4 v[138:141], v[172:175], v[208:211], v[138:141] cbsz:4 blgp:4
	v_mfma_f32_16x16x128_f8f6f4 v[82:85], v[168:171], v[200:203], v[82:85] cbsz:4 blgp:4
	s_nop 0
	v_mfma_f32_16x16x128_f8f6f4 v[82:85], v[176:179], v[208:211], v[82:85] cbsz:4 blgp:4
	v_mfma_f32_16x16x128_f8f6f4 v[94:97], v[212:215], v[180:183], v[94:97] cbsz:4 blgp:4
	s_nop 0
	v_mfma_f32_16x16x128_f8f6f4 v[94:97], v[220:223], v[188:191], v[94:97] cbsz:4 blgp:4
	v_mfma_f32_16x16x128_f8f6f4 v[102:105], v[216:219], v[180:183], v[102:105] cbsz:4 blgp:4
	s_nop 0
	v_mfma_f32_16x16x128_f8f6f4 v[102:105], v[224:227], v[188:191], v[102:105] cbsz:4 blgp:4
	v_mfma_f32_16x16x128_f8f6f4 v[110:113], v[212:215], v[184:187], v[110:113] cbsz:4 blgp:4
	s_nop 0
	v_mfma_f32_16x16x128_f8f6f4 v[110:113], v[220:223], v[192:195], v[110:113] cbsz:4 blgp:4
	v_mfma_f32_16x16x128_f8f6f4 v[114:117], v[216:219], v[184:187], v[114:117] cbsz:4 blgp:4
	s_nop 0
	v_mfma_f32_16x16x128_f8f6f4 v[114:117], v[224:227], v[192:195], v[114:117] cbsz:4 blgp:4
	v_mfma_f32_16x16x128_f8f6f4 v[122:125], v[212:215], v[196:199], v[122:125] cbsz:4 blgp:4
	s_nop 0
	v_mfma_f32_16x16x128_f8f6f4 v[122:125], v[220:223], v[204:207], v[122:125] cbsz:4 blgp:4
	v_mfma_f32_16x16x128_f8f6f4 v[130:133], v[216:219], v[196:199], v[130:133] cbsz:4 blgp:4
	s_nop 0
	v_mfma_f32_16x16x128_f8f6f4 v[130:133], v[224:227], v[204:207], v[130:133] cbsz:4 blgp:4
	v_mfma_f32_16x16x128_f8f6f4 v[134:137], v[212:215], v[200:203], v[134:137] cbsz:4 blgp:4
	s_nop 0
	v_mfma_f32_16x16x128_f8f6f4 v[134:137], v[220:223], v[208:211], v[134:137] cbsz:4 blgp:4
	v_mfma_f32_16x16x128_f8f6f4 v[142:145], v[216:219], v[200:203], v[142:145] cbsz:4 blgp:4
	s_nop 0
	v_mfma_f32_16x16x128_f8f6f4 v[142:145], v[224:227], v[208:211], v[142:145] cbsz:4 blgp:4
	s_setprio 0
	s_andn2_b64 vcc, exec, s[34:35]
	s_barrier
	s_cbranch_vccnz .LBB5_4
	s_ashr_i32 s29, s28, 31
	s_lshl_b64 s[44:45], s[28:29], 10
	s_add_u32 s44, s10, s44
	s_addc_u32 s45, s11, s45
	s_add_u32 s29, s42, 0x200
	s_addc_u32 s79, s43, 0
	s_add_u32 s80, s40, 0x200
	s_addc_u32 s81, s41, 0
	s_add_u32 s40, s82, 0x180
	s_addc_u32 s41, s83, 0
	s_mov_b32 s82, 4
	s_cmp_eq_u32 s64, s82
	s_cselect_b64 s[42:43], -1, 0
	s_cmp_lg_u32 s64, s82
	s_cbranch_scc1 .LBB5_15

	.amdhsa_kernel _Z6k_gemmI4Epi8ILi1ELb1ELb1EEEv4GemmT_iiii
		.amdhsa_group_segment_fixed_size 0
		.amdhsa_private_segment_fixed_size 0
		.amdhsa_kernarg_size 328
		.amdhsa_user_sgpr_count 2
		.amdhsa_user_sgpr_dispatch_ptr 0
		.amdhsa_user_sgpr_queue_ptr 0
		.amdhsa_user_sgpr_kernarg_segment_ptr 1
		.amdhsa_user_sgpr_dispatch_id 0
		.amdhsa_user_sgpr_kernarg_preload_length 0
		.amdhsa_user_sgpr_kernarg_preload_offset 0
		.amdhsa_user_sgpr_private_segment_size 0
		.amdhsa_uses_dynamic_stack 0
		.amdhsa_enable_private_segment 0
		.amdhsa_system_sgpr_workgroup_id_x 1
		.amdhsa_system_sgpr_workgroup_id_y 0
		.amdhsa_system_sgpr_workgroup_id_z 0
		.amdhsa_system_sgpr_workgroup_info 0
		.amdhsa_system_vgpr_workitem_id 0
		.amdhsa_next_free_vgpr 232
		.amdhsa_next_free_sgpr 84
		.amdhsa_accum_offset 232
		.amdhsa_reserve_vcc 1
		.amdhsa_float_round_mode_32 0
		.amdhsa_float_round_mode_16_64 0
		.amdhsa_float_denorm_mode_32 3
		.amdhsa_float_denorm_mode_16_64 3
		.amdhsa_dx10_clamp 1
		.amdhsa_ieee_mode 1
		.amdhsa_fp16_overflow 0
		.amdhsa_tg_split 0
		.amdhsa_exception_fp_ieee_invalid_op 0
		.amdhsa_exception_fp_denorm_src 0
		.amdhsa_exception_fp_ieee_div_zero 0
		.amdhsa_exception_fp_ieee_overflow 0
		.amdhsa_exception_fp_ieee_underflow 0
		.amdhsa_exception_fp_ieee_inexact 0
		.amdhsa_exception_int_div_zero 0
	.end_amdhsa_kernel

amdhsa.kernels:
  - .agpr_count:     0
    .args:
      - .offset:         0
        .size:           80
        .value_kind:     by_value
    .group_segment_fixed_size: 8192
    .kernarg_segment_align: 8
    .kernarg_segment_size: 80
    .language:       OpenCL C
    .language_version:
      - 2
      - 0
    .max_flat_workgroup_size: 256
    .name:           _Z6k_prep8PrepArgs
    .private_segment_fixed_size: 0
    .sgpr_count:     35
    .sgpr_spill_count: 0
    .symbol:         _Z6k_prep8PrepArgs.kd
    .uniform_work_group_size: 1
    .uses_dynamic_stack: false
    .vgpr_count:     45
    .vgpr_spill_count: 0
    .wavefront_size: 64
  - .agpr_count:     4
    .args:
      - .actual_access:  read_only
        .address_space:  global
        .offset:         0
        .size:           8
        .value_kind:     global_buffer
      - .actual_access:  read_only
        .address_space:  global
        .offset:         8
        .size:           8
        .value_kind:     global_buffer
      - .actual_access:  read_only
        .address_space:  global
        .offset:         16
        .size:           8
        .value_kind:     global_buffer
      - .actual_access:  write_only
        .address_space:  global
        .offset:         24
        .size:           8
        .value_kind:     global_buffer
      - .actual_access:  write_only
        .address_space:  global
        .offset:         32
        .size:           8
        .value_kind:     global_buffer
    .group_segment_fixed_size: 36096
    .kernarg_segment_align: 8
    .kernarg_segment_size: 40
    .language:       OpenCL C
    .language_version:
      - 2
      - 0
    .max_flat_workgroup_size: 256
    .name:           _Z7k_gatesPKfPKtS0_PhPf
    .private_segment_fixed_size: 0
    .sgpr_count:     18
    .sgpr_spill_count: 0
    .symbol:         _Z7k_gatesPKfPKtS0_PhPf.kd
    .uniform_work_group_size: 1
    .uses_dynamic_stack: false
    .vgpr_count:     88
    .vgpr_spill_count: 0
    .wavefront_size: 64
  - .agpr_count:     0
    .args:
      - .actual_access:  read_only
        .address_space:  global
        .offset:         0
        .size:           8
        .value_kind:     global_buffer
      - .actual_access:  read_only
        .address_space:  global
        .offset:         8
        .size:           8
        .value_kind:     global_buffer
      - .actual_access:  write_only
        .address_space:  global
        .offset:         16
        .size:           8
        .value_kind:     global_buffer
      - .offset:         24
        .size:           4
        .value_kind:     by_value
    .group_segment_fixed_size: 0
    .kernarg_segment_align: 8
    .kernarg_segment_size: 28
    .language:       OpenCL C
    .language_version:
      - 2
      - 0
    .max_flat_workgroup_size: 256
    .name:           _Z5k_mixPKhPKfPhi
    .private_segment_fixed_size: 0
    .sgpr_count:     14
    .sgpr_spill_count: 0
    .symbol:         _Z5k_mixPKhPKfPhi.kd
    .uniform_work_group_size: 1
    .uses_dynamic_stack: false
    .vgpr_count:     126
    .vgpr_spill_count: 0
    .wavefront_size: 64
  - .agpr_count:     0
    .args:
      - .actual_access:  read_only
        .address_space:  global
        .offset:         0
        .size:           8
        .value_kind:     global_buffer
      - .actual_access:  read_only
        .address_space:  global
        .offset:         8
        .size:           8
        .value_kind:     global_buffer
      - .actual_access:  write_only
        .address_space:  global
        .offset:         16
        .size:           8
        .value_kind:     global_buffer
    .group_segment_fixed_size: 0
    .kernarg_segment_align: 8
    .kernarg_segment_size: 24
    .language:       OpenCL C
    .language_version:
      - 2
      - 0
    .max_flat_workgroup_size: 256
    .name:           _Z7k_finalPKfS0_Pf
    .private_segment_fixed_size: 0
    .sgpr_count:     16
    .sgpr_spill_count: 0
    .symbol:         _Z7k_finalPKfS0_Pf.kd
    .uniform_work_group_size: 1
    .uses_dynamic_stack: false
    .vgpr_count:     16
    .vgpr_spill_count: 0
    .wavefront_size: 64
  - .agpr_count:     0
    .args:
      - .offset:         0
        .size:           24
        .value_kind:     by_value
      - .offset:         24
        .size:           32
        .value_kind:     by_value
      - .offset:         56
        .size:           4
        .value_kind:     by_value
      - .offset:         60
        .size:           4
        .value_kind:     by_value
      - .offset:         64
        .size:           4
        .value_kind:     by_value
      - .offset:         68
        .size:           4
        .value_kind:     by_value
      - .offset:         72
        .size:           4
        .value_kind:     hidden_block_count_x
      - .offset:         76
        .size:           4
        .value_kind:     hidden_block_count_y
      - .offset:         80
        .size:           4
        .value_kind:     hidden_block_count_z
      - .offset:         84
        .size:           2
        .value_kind:     hidden_group_size_x
      - .offset:         86
        .size:           2
        .value_kind:     hidden_group_size_y
      - .offset:         88
        .size:           2
        .value_kind:     hidden_group_size_z
      - .offset:         90
        .size:           2
        .value_kind:     hidden_remainder_x
      - .offset:         92
        .size:           2
        .value_kind:     hidden_remainder_y
      - .offset:         94
        .size:           2
        .value_kind:     hidden_remainder_z
      - .offset:         112
        .size:           8
        .value_kind:     hidden_global_offset_x
      - .offset:         120
        .size:           8
        .value_kind:     hidden_global_offset_y
      - .offset:         128
        .size:           8
        .value_kind:     hidden_global_offset_z
      - .offset:         136
        .size:           2
        .value_kind:     hidden_grid_dims
      - .offset:         192
        .size:           4
        .value_kind:     hidden_dynamic_lds_size
    .group_segment_fixed_size: 0
    .kernarg_segment_align: 8
    .kernarg_segment_size: 328
    .language:       OpenCL C
    .language_version:
      - 2
      - 0
    .max_flat_workgroup_size: 512
    .name:           _Z6k_gemmI4Epi8ILi0ELb1ELb1EEEv4GemmT_iiii
    .private_segment_fixed_size: 0
    .sgpr_count:     89
    .sgpr_spill_count: 0
    .symbol:         _Z6k_gemmI4Epi8ILi0ELb1ELb1EEEv4GemmT_iiii.kd
    .uniform_work_group_size: 1
    .uses_dynamic_stack: false
    .vgpr_count:     230
    .vgpr_spill_count: 0
    .wavefront_size: 64
  - .agpr_count:     0
    .args:
      - .offset:         0
        .size:           24
        .value_kind:     by_value
      - .offset:         24
        .size:           32
        .value_kind:     by_value
      - .offset:         56
        .size:           4
        .value_kind:     by_value
      - .offset:         60
        .size:           4
        .value_kind:     by_value
      - .offset:         64
        .size:           4
        .value_kind:     by_value
      - .offset:         68
        .size:           4
        .value_kind:     by_value
      - .offset:         72
        .size:           4
        .value_kind:     hidden_block_count_x
      - .offset:         76
        .size:           4
        .value_kind:     hidden_block_count_y
      - .offset:         80
        .size:           4
        .value_kind:     hidden_block_count_z
      - .offset:         84
        .size:           2
        .value_kind:     hidden_group_size_x
      - .offset:         86
        .size:           2
        .value_kind:     hidden_group_size_y
      - .offset:         88
        .size:           2
        .value_kind:     hidden_group_size_z
      - .offset:         90
        .size:           2
        .value_kind:     hidden_remainder_x
      - .offset:         92
        .size:           2
        .value_kind:     hidden_remainder_y
      - .offset:         94
        .size:           2
        .value_kind:     hidden_remainder_z
      - .offset:         112
        .size:           8
        .value_kind:     hidden_global_offset_x
      - .offset:         120
        .size:           8
        .value_kind:     hidden_global_offset_y
      - .offset:         128
        .size:           8
        .value_kind:     hidden_global_offset_z
      - .offset:         136
        .size:           2
        .value_kind:     hidden_grid_dims
      - .offset:         192
        .size:           4
        .value_kind:     hidden_dynamic_lds_size
    .group_segment_fixed_size: 0
    .kernarg_segment_align: 8
    .kernarg_segment_size: 328
    .language:       OpenCL C
    .language_version:
      - 2
      - 0
    .max_flat_workgroup_size: 512
    .name:           _Z6k_gemmI4Epi8ILi1ELb1ELb1EEEv4GemmT_iiii
    .private_segment_fixed_size: 0
    .sgpr_count:     90
    .sgpr_spill_count: 0
    .symbol:         _Z6k_gemmI4Epi8ILi1ELb1ELb1EEEv4GemmT_iiii.kd
    .uniform_work_group_size: 1
    .uses_dynamic_stack: false
    .vgpr_count:     232
    .vgpr_spill_count: 0
    .wavefront_size: 64
  - .agpr_count:     0
    .args:
      - .offset:         0
        .size:           24
        .value_kind:     by_value
      - .offset:         24
        .size:           32
        .value_kind:     by_value
      - .offset:         56
        .size:           4
        .value_kind:     by_value
      - .offset:         60
        .size:           4
        .value_kind:     by_value
      - .offset:         64
        .size:           4
        .value_kind:     by_value
      - .offset:         68
        .size:           4
        .value_kind:     by_value
      - .offset:         72
        .size:           4
        .value_kind:     hidden_block_count_x
      - .offset:         76
        .size:           4
        .value_kind:     hidden_block_count_y
      - .offset:         80
        .size:           4
        .value_kind:     hidden_block_count_z
      - .offset:         84
        .size:           2
        .value_kind:     hidden_group_size_x
      - .offset:         86
        .size:           2
        .value_kind:     hidden_group_size_y
      - .offset:         88
        .size:           2
        .value_kind:     hidden_group_size_z
      - .offset:         90
        .size:           2
        .value_kind:     hidden_remainder_x
      - .offset:         92
        .size:           2
        .value_kind:     hidden_remainder_y
      - .offset:         94
        .size:           2
        .value_kind:     hidden_remainder_z
      - .offset:         112
        .size:           8
        .value_kind:     hidden_global_offset_x
      - .offset:         120
        .size:           8
        .value_kind:     hidden_global_offset_y
      - .offset:         128
        .size:           8
        .value_kind:     hidden_global_offset_z
      - .offset:         136
        .size:           2
        .value_kind:     hidden_grid_dims
      - .offset:         192
        .size:           4
        .value_kind:     hidden_dynamic_lds_size
    .group_segment_fixed_size: 0
    .kernarg_segment_align: 8
    .kernarg_segment_size: 328
    .language:       OpenCL C
    .language_version:
      - 2
      - 0
    .max_flat_workgroup_size: 512
    .name:           _Z6k_gemmI8EpiTowerEv4GemmT_iiii
    .private_segment_fixed_size: 0
    .sgpr_count:     92
    .sgpr_spill_count: 0
    .symbol:         _Z6k_gemmI8EpiTowerEv4GemmT_iiii.kd
    .uniform_work_group_size: 1
    .uses_dynamic_stack: false
    .vgpr_count:     230
    .vgpr_spill_count: 0
    .wavefront_size: 64
